# baseline (speedup 1.0000x reference)
_Z5k_decPKiPKDF16_S2_PKfS4_S4_Pf:
	s_load_dword s3, s[0:1], 0x44
	s_load_dword s6, s[0:1], 0x38
	s_load_dwordx2 s[4:5], s[0:1], 0x0
	s_load_dwordx8 s[28:35], s[0:1], 0x8
	s_load_dwordx4 s[12:15], s[0:1], 0x28
	v_and_b32_e32 v1, 15, v0
	v_and_b32_e32 v64, 63, v0
	v_lshlrev_b32_e32 v96, 3, v1
	v_lshrrev_b32_e32 v4, 3, v0
	v_and_b32_e32 v4, 4, v4
	v_or_b32_e32 v96, v96, v4
	v_mov_b32_e32 v97, 0
	v_and_b32_e32 v104, 16, v0
	v_lshlrev_b32_e32 v6, 7, v0
	v_lshlrev_b32_e32 v7, 2, v64
	s_movk_i32 s16, 0x6000
	v_and_or_b32 v103, v6, s16, v7
	v_mov_b32_e32 v219, 0
	s_movk_i32 s19, 0x3d08
	s_waitcnt lgkmcnt(0)
	s_and_b32 s3, s3, 0xffff
	s_mul_i32 s2, s2, s3
	v_add_u32_e32 v5, s2, v0
	s_mul_i32 s6, s6, s3
	v_lshrrev_b32_e32 v102, 6, v5
	s_lshr_b32 s18, s6, 6
	v_readfirstlane_b32 s23, v102
	v_lshl_add_u64 v[2:3], s[4:5], 0, v[96:97]
	s_mov_b32 s16, 0xf4240
	v_cmp_gt_u32_e32 vcc, s16, v5
	s_and_saveexec_b64 s[22:23], vcc
	s_cbranch_execz .LBB2_3
	v_mov_b32_e32 v222, v2
	v_mov_b32_e32 v223, v3
	v_min_u32_e32 v218, s19, v102
	v_lshlrev_b32_e32 v218, 9, v218
	v_lshl_add_u64 v[216:217], v[222:223], 0, v[218:219]
	global_load_dword v65, v[216:217], off nt
	global_load_dword v80, v[216:217], off offset:128 nt
	global_load_dword v81, v[216:217], off offset:256 nt
	global_load_dword v82, v[216:217], off offset:384 nt
	v_add_u32_e32 v220, s18, v102
	v_min_u32_e32 v218, s19, v220
	v_lshlrev_b32_e32 v218, 9, v218
	v_lshl_add_u64 v[216:217], v[222:223], 0, v[218:219]
	global_load_dword v100, v[216:217], off nt
	global_load_dword v101, v[216:217], off offset:128 nt
	global_load_dword v98, v[216:217], off offset:256 nt
	global_load_dword v99, v[216:217], off offset:384 nt
	s_mov_b32 s8, s28
	s_and_b32 s9, s29, 0xffff
	s_mov_b32 s10, 0x30d400
	s_mov_b32 s11, 0x20000
	s_mov_b64 s[36:37], 0x1000
	v_and_b32_e32 v96, 48, v64
	v_lshlrev_b32_e32 v221, 6, v1
	v_lshlrev_b32_e32 v211, 2, v1
	v_lshlrev_b32_e32 v214, 4, v0
	v_add_u32_e32 v215, 0x1000, v214
	v_mul_u32_u24_e32 v134, 0x50, v1
	v_add_u32_e32 v134, v134, v96
	v_add_u32_e32 v134, 0x9000, v134
	v_and_b32_e32 v135, 3, v0
	v_lshlrev_b32_e32 v135, 4, v135
	v_lshrrev_b32_e32 v133, 2, v0
	v_mul_u32_u24_e32 v133, 0x50, v133
	v_add_u32_e32 v133, v133, v135
	v_add_u32_e32 v133, 0x9000, v133
	v_lshl_or_b32 v221, v102, 6, v64
	v_lshrrev_b32_e32 v213, 4, v64
	v_cmp_gt_u32_e32 vcc, 16, v64
	v_and_b32_e32 v210, 31, v64
	v_lshlrev_b32_e32 v210, 4, v210
	s_mov_b32 s38, -1
	s_mov_b32 s39, 0
	s_mov_b64 exec, s[38:39]
	global_load_dwordx4 v[126:129], v210, s[32:33]
	s_mov_b32 s38, 0
	s_mov_b32 s39, -1
	s_mov_b64 exec, s[38:39]
	global_load_dwordx4 v[126:129], v210, s[34:35]
	s_mov_b64 exec, -1
	global_load_dwordx4 v[32:35], v214, s[30:31]
	global_load_dwordx4 v[36:39], v215, s[30:31]
	s_load_dword s12, s[12:13], 0x0
	s_waitcnt vmcnt(8)
	v_lshl_or_b32 v216, v65, 5, v104
	v_lshl_or_b32 v217, v80, 5, v104
	v_lshl_or_b32 v218, v81, 5, v104
	v_lshl_or_b32 v212, v82, 5, v104
	buffer_load_dwordx4 v[92:95], v216, s[8:11], 0 offen
	buffer_load_dwordx4 v[88:91], v217, s[8:11], 0 offen
	buffer_load_dwordx4 v[84:87], v218, s[8:11], 0 offen
	buffer_load_dwordx4 v[80:83], v212, s[8:11], 0 offen
	s_lshl_b32 s21, s18, 6
	s_mov_b32 s20, 2
	s_mov_b64 s[16:17], 0
	v_cmp_eq_u32_e64 s[0:1], 1, v213
	v_cmp_eq_u32_e64 s[2:3], 2, v213
	v_cmp_eq_u32_e64 s[4:5], 3, v213
	v_mov_b32_e32 v96, v221
	v_mov_b32_e32 v97, 0
	s_waitcnt vmcnt(6)
	v_lshrrev_b32_e32 v210, 6, v0
	v_lshlrev_b32_e32 v210, 10, v210
	v_add_u32_e32 v210, 0x8000, v210
	v_lshl_add_u32 v130, v64, 4, v210
	v_lshl_add_u32 v131, v213, 4, v210
	v_add_u32_e32 v132, v211, v210
	ds_write_b128 v130, v[126:129]
	ds_read_b128 v[68:71], v131 offset:512
	ds_read_b128 v[72:75], v131 offset:576
	ds_read_b128 v[76:79], v131 offset:640
	ds_read_b128 v[106:109], v131 offset:704
	ds_read_b128 v[110:113], v131 offset:768
	ds_read_b128 v[114:117], v131 offset:832
	ds_read_b128 v[118:121], v131 offset:896
	ds_read_b128 v[122:125], v131 offset:960
	s_waitcnt lgkmcnt(0)
	s_waitcnt vmcnt(4)
	ds_write_b128 v133, v[32:35]
	ds_write_b128 v133, v[36:39] offset:5120
	ds_read_b32 v148, v132 offset:512
	ds_read_b32 v149, v132 offset:576
	ds_read_b32 v150, v132 offset:640
	ds_read_b32 v151, v132 offset:704
	ds_read_b32 v152, v132 offset:768
	ds_read_b32 v153, v132 offset:832
	ds_read_b32 v154, v132 offset:896
	ds_read_b32 v155, v132 offset:960
	ds_read_b32 v156, v132 offset:0
	ds_read_b32 v157, v132 offset:64
	ds_read_b32 v158, v132 offset:128
	ds_read_b32 v159, v132 offset:192
	s_waitcnt lgkmcnt(0)
	ds_read_b32 v160, v132 offset:256
	ds_read_b32 v161, v132 offset:320
	ds_read_b32 v162, v132 offset:384
	ds_read_b32 v163, v132 offset:448
	ds_read_b128 v[0:3], v131 offset:0
	ds_read_b128 v[4:7], v131 offset:64
	ds_read_b128 v[8:11], v131 offset:128
	ds_read_b128 v[12:15], v131 offset:192
	ds_read_b128 v[16:19], v131 offset:256
	ds_read_b128 v[20:23], v131 offset:320
	ds_read_b128 v[24:27], v131 offset:384
	ds_read_b128 v[28:31], v131 offset:448
	s_waitcnt lgkmcnt(0)
	s_barrier
	ds_read_b128 v[32:35], v134
	ds_read_b128 v[36:39], v134 offset:1280
	ds_read_b128 v[40:43], v134 offset:2560
	ds_read_b128 v[44:47], v134 offset:3840
	ds_read_b128 v[48:51], v134 offset:5120
	ds_read_b128 v[52:55], v134 offset:6400
	ds_read_b128 v[56:59], v134 offset:7680
	ds_read_b128 v[60:63], v134 offset:8960
	v_cvt_pk_f16_f32 v67, v74, v75
	v_cvt_pk_f16_f32 v66, v72, v73
	v_cvt_pk_f16_f32 v65, v70, v71
	v_cvt_pk_f16_f32 v64, v68, v69
	v_cvt_pk_f16_f32 v71, v108, v109
	v_cvt_pk_f16_f32 v70, v106, v107
	v_cvt_pk_f16_f32 v69, v78, v79
	v_cvt_pk_f16_f32 v68, v76, v77
	v_cvt_pk_f16_f32 v75, v116, v117
	v_cvt_pk_f16_f32 v74, v114, v115
	v_cvt_pk_f16_f32 v73, v112, v113
	v_cvt_pk_f16_f32 v72, v110, v111
	v_cvt_pk_f16_f32 v79, v124, v125
	v_cvt_pk_f16_f32 v78, v122, v123
	v_cvt_pk_f16_f32 v77, v120, v121
	v_cvt_pk_f16_f32 v76, v118, v119
	v_mov_b32_e32 v167, 0x38003800
	v_pk_mul_f16 v64, v64, v167
	v_pk_mul_f16 v65, v65, v167
	v_pk_mul_f16 v66, v66, v167
	v_pk_mul_f16 v67, v67, v167
	v_pk_mul_f16 v68, v68, v167
	v_pk_mul_f16 v69, v69, v167
	v_pk_mul_f16 v70, v70, v167
	v_pk_mul_f16 v71, v71, v167
	v_pk_mul_f16 v72, v72, v167
	v_pk_mul_f16 v73, v73, v167
	v_pk_mul_f16 v74, v74, v167
	v_pk_mul_f16 v75, v75, v167
	v_pk_mul_f16 v76, v76, v167
	v_pk_mul_f16 v77, v77, v167
	v_pk_mul_f16 v78, v78, v167
	v_pk_mul_f16 v79, v79, v167
	v_cvt_f16_f32_e32 v148, v148
	v_cvt_f16_f32_e32 v149, v149
	v_cvt_f16_f32_e32 v150, v150
	v_cvt_f16_f32_e32 v151, v151
	v_cvt_f16_f32_e32 v152, v152
	v_cvt_f16_f32_e32 v153, v153
	v_cvt_f16_f32_e32 v154, v154
	v_cvt_f16_f32_e32 v155, v155
	v_cvt_f32_f16_e32 v148, v148
	v_cvt_f32_f16_e32 v149, v149
	v_cvt_f32_f16_e32 v150, v150
	v_cvt_f32_f16_e32 v151, v151
	v_cvt_f32_f16_e32 v152, v152
	v_cvt_f32_f16_e32 v153, v153
	v_cvt_f32_f16_e32 v154, v154
	v_cvt_f32_f16_e32 v155, v155
	v_mul_f32_e32 v148, 0.5, v148
	v_mul_f32_e32 v149, 0.5, v149
	v_mul_f32_e32 v150, 0.5, v150
	v_mul_f32_e32 v151, 0.5, v151
	v_mul_f32_e32 v152, 0.5, v152
	v_mul_f32_e32 v153, 0.5, v153
	v_mul_f32_e32 v154, 0.5, v154
	v_mul_f32_e32 v155, 0.5, v155
	v_mov_b32_e32 v140, 0
	v_mov_b32_e32 v141, 0
	v_mov_b32_e32 v142, 0
	v_mov_b32_e32 v143, 0
	v_mov_b32_e32 v144, 0
	v_mov_b32_e32 v145, 0
	v_mov_b32_e32 v146, 0
	v_mov_b32_e32 v147, 0
	v_mov_b32_e32 v166, 0
	s_waitcnt lgkmcnt(0)
	v_cvt_f32_f16_e32 v164, v32
	v_cvt_f32_f16_sdwa v165, v32 dst_sel:DWORD dst_unused:UNUSED_PAD src0_sel:WORD_1
	v_fmac_f32_e32 v140, v148, v164
	v_fmac_f32_e32 v141, v148, v165
	v_cvt_f32_f16_e32 v164, v33
	v_cvt_f32_f16_sdwa v165, v33 dst_sel:DWORD dst_unused:UNUSED_PAD src0_sel:WORD_1
	v_fmac_f32_e32 v142, v148, v164
	v_fmac_f32_e32 v143, v148, v165
	v_cvt_f32_f16_e32 v164, v34
	v_cvt_f32_f16_sdwa v165, v34 dst_sel:DWORD dst_unused:UNUSED_PAD src0_sel:WORD_1
	v_fmac_f32_e32 v144, v148, v164
	v_fmac_f32_e32 v145, v148, v165
	v_cvt_f32_f16_e32 v164, v35
	v_cvt_f32_f16_sdwa v165, v35 dst_sel:DWORD dst_unused:UNUSED_PAD src0_sel:WORD_1
	v_fmac_f32_e32 v146, v148, v164
	v_fmac_f32_e32 v147, v148, v165
	v_fmac_f32_e32 v166, v148, v156
	v_cvt_f32_f16_e32 v164, v36
	v_cvt_f32_f16_sdwa v165, v36 dst_sel:DWORD dst_unused:UNUSED_PAD src0_sel:WORD_1
	v_fmac_f32_e32 v140, v149, v164
	v_fmac_f32_e32 v141, v149, v165
	v_cvt_f32_f16_e32 v164, v37
	v_cvt_f32_f16_sdwa v165, v37 dst_sel:DWORD dst_unused:UNUSED_PAD src0_sel:WORD_1
	v_fmac_f32_e32 v142, v149, v164
	v_fmac_f32_e32 v143, v149, v165
	v_cvt_f32_f16_e32 v164, v38
	v_cvt_f32_f16_sdwa v165, v38 dst_sel:DWORD dst_unused:UNUSED_PAD src0_sel:WORD_1
	v_fmac_f32_e32 v144, v149, v164
	v_fmac_f32_e32 v145, v149, v165
	v_cvt_f32_f16_e32 v164, v39
	v_cvt_f32_f16_sdwa v165, v39 dst_sel:DWORD dst_unused:UNUSED_PAD src0_sel:WORD_1
	v_fmac_f32_e32 v146, v149, v164
	v_fmac_f32_e32 v147, v149, v165
	v_fmac_f32_e32 v166, v149, v157
	v_cvt_f32_f16_e32 v164, v40
	v_cvt_f32_f16_sdwa v165, v40 dst_sel:DWORD dst_unused:UNUSED_PAD src0_sel:WORD_1
	v_fmac_f32_e32 v140, v150, v164
	v_fmac_f32_e32 v141, v150, v165
	v_cvt_f32_f16_e32 v164, v41
	v_cvt_f32_f16_sdwa v165, v41 dst_sel:DWORD dst_unused:UNUSED_PAD src0_sel:WORD_1
	v_fmac_f32_e32 v142, v150, v164
	v_fmac_f32_e32 v143, v150, v165
	v_cvt_f32_f16_e32 v164, v42
	v_cvt_f32_f16_sdwa v165, v42 dst_sel:DWORD dst_unused:UNUSED_PAD src0_sel:WORD_1
	v_fmac_f32_e32 v144, v150, v164
	v_fmac_f32_e32 v145, v150, v165
	v_cvt_f32_f16_e32 v164, v43
	v_cvt_f32_f16_sdwa v165, v43 dst_sel:DWORD dst_unused:UNUSED_PAD src0_sel:WORD_1
	v_fmac_f32_e32 v146, v150, v164
	v_fmac_f32_e32 v147, v150, v165
	v_fmac_f32_e32 v166, v150, v158
	v_cvt_f32_f16_e32 v164, v44
	v_cvt_f32_f16_sdwa v165, v44 dst_sel:DWORD dst_unused:UNUSED_PAD src0_sel:WORD_1
	v_fmac_f32_e32 v140, v151, v164
	v_fmac_f32_e32 v141, v151, v165
	v_cvt_f32_f16_e32 v164, v45
	v_cvt_f32_f16_sdwa v165, v45 dst_sel:DWORD dst_unused:UNUSED_PAD src0_sel:WORD_1
	v_fmac_f32_e32 v142, v151, v164
	v_fmac_f32_e32 v143, v151, v165
	v_cvt_f32_f16_e32 v164, v46
	v_cvt_f32_f16_sdwa v165, v46 dst_sel:DWORD dst_unused:UNUSED_PAD src0_sel:WORD_1
	v_fmac_f32_e32 v144, v151, v164
	v_fmac_f32_e32 v145, v151, v165
	v_cvt_f32_f16_e32 v164, v47
	v_cvt_f32_f16_sdwa v165, v47 dst_sel:DWORD dst_unused:UNUSED_PAD src0_sel:WORD_1
	v_fmac_f32_e32 v146, v151, v164
	v_fmac_f32_e32 v147, v151, v165
	v_fmac_f32_e32 v166, v151, v159
	v_cvt_f32_f16_e32 v164, v48
	v_cvt_f32_f16_sdwa v165, v48 dst_sel:DWORD dst_unused:UNUSED_PAD src0_sel:WORD_1
	v_fmac_f32_e32 v140, v152, v164
	v_fmac_f32_e32 v141, v152, v165
	v_cvt_f32_f16_e32 v164, v49
	v_cvt_f32_f16_sdwa v165, v49 dst_sel:DWORD dst_unused:UNUSED_PAD src0_sel:WORD_1
	v_fmac_f32_e32 v142, v152, v164
	v_fmac_f32_e32 v143, v152, v165
	v_cvt_f32_f16_e32 v164, v50
	v_cvt_f32_f16_sdwa v165, v50 dst_sel:DWORD dst_unused:UNUSED_PAD src0_sel:WORD_1
	v_fmac_f32_e32 v144, v152, v164
	v_fmac_f32_e32 v145, v152, v165
	v_cvt_f32_f16_e32 v164, v51
	v_cvt_f32_f16_sdwa v165, v51 dst_sel:DWORD dst_unused:UNUSED_PAD src0_sel:WORD_1
	v_fmac_f32_e32 v146, v152, v164
	v_fmac_f32_e32 v147, v152, v165
	v_fmac_f32_e32 v166, v152, v160
	v_cvt_f32_f16_e32 v164, v52
	v_cvt_f32_f16_sdwa v165, v52 dst_sel:DWORD dst_unused:UNUSED_PAD src0_sel:WORD_1
	v_fmac_f32_e32 v140, v153, v164
	v_fmac_f32_e32 v141, v153, v165
	v_cvt_f32_f16_e32 v164, v53
	v_cvt_f32_f16_sdwa v165, v53 dst_sel:DWORD dst_unused:UNUSED_PAD src0_sel:WORD_1
	v_fmac_f32_e32 v142, v153, v164
	v_fmac_f32_e32 v143, v153, v165
	v_cvt_f32_f16_e32 v164, v54
	v_cvt_f32_f16_sdwa v165, v54 dst_sel:DWORD dst_unused:UNUSED_PAD src0_sel:WORD_1
	v_fmac_f32_e32 v144, v153, v164
	v_fmac_f32_e32 v145, v153, v165
	v_cvt_f32_f16_e32 v164, v55
	v_cvt_f32_f16_sdwa v165, v55 dst_sel:DWORD dst_unused:UNUSED_PAD src0_sel:WORD_1
	v_fmac_f32_e32 v146, v153, v164
	v_fmac_f32_e32 v147, v153, v165
	v_fmac_f32_e32 v166, v153, v161
	v_cvt_f32_f16_e32 v164, v56
	v_cvt_f32_f16_sdwa v165, v56 dst_sel:DWORD dst_unused:UNUSED_PAD src0_sel:WORD_1
	v_fmac_f32_e32 v140, v154, v164
	v_fmac_f32_e32 v141, v154, v165
	v_cvt_f32_f16_e32 v164, v57
	v_cvt_f32_f16_sdwa v165, v57 dst_sel:DWORD dst_unused:UNUSED_PAD src0_sel:WORD_1
	v_fmac_f32_e32 v142, v154, v164
	v_fmac_f32_e32 v143, v154, v165
	v_cvt_f32_f16_e32 v164, v58
	v_cvt_f32_f16_sdwa v165, v58 dst_sel:DWORD dst_unused:UNUSED_PAD src0_sel:WORD_1
	v_fmac_f32_e32 v144, v154, v164
	v_fmac_f32_e32 v145, v154, v165
	v_cvt_f32_f16_e32 v164, v59
	v_cvt_f32_f16_sdwa v165, v59 dst_sel:DWORD dst_unused:UNUSED_PAD src0_sel:WORD_1
	v_fmac_f32_e32 v146, v154, v164
	v_fmac_f32_e32 v147, v154, v165
	v_fmac_f32_e32 v166, v154, v162
	v_cvt_f32_f16_e32 v164, v60
	v_cvt_f32_f16_sdwa v165, v60 dst_sel:DWORD dst_unused:UNUSED_PAD src0_sel:WORD_1
	v_fmac_f32_e32 v140, v155, v164
	v_fmac_f32_e32 v141, v155, v165
	v_cvt_f32_f16_e32 v164, v61
	v_cvt_f32_f16_sdwa v165, v61 dst_sel:DWORD dst_unused:UNUSED_PAD src0_sel:WORD_1
	v_fmac_f32_e32 v142, v155, v164
	v_fmac_f32_e32 v143, v155, v165
	v_cvt_f32_f16_e32 v164, v62
	v_cvt_f32_f16_sdwa v165, v62 dst_sel:DWORD dst_unused:UNUSED_PAD src0_sel:WORD_1
	v_fmac_f32_e32 v144, v155, v164
	v_fmac_f32_e32 v145, v155, v165
	v_cvt_f32_f16_e32 v164, v63
	v_cvt_f32_f16_sdwa v165, v63 dst_sel:DWORD dst_unused:UNUSED_PAD src0_sel:WORD_1
	v_fmac_f32_e32 v146, v155, v164
	v_fmac_f32_e32 v147, v155, v165
	v_fmac_f32_e32 v166, v155, v163
	v_add_f32_dpp v140, v140, v140 row_ror:8 row_mask:0xf bank_mask:0xf
	v_add_f32_dpp v141, v141, v141 row_ror:8 row_mask:0xf bank_mask:0xf
	v_add_f32_dpp v142, v142, v142 row_ror:8 row_mask:0xf bank_mask:0xf
	v_add_f32_dpp v143, v143, v143 row_ror:8 row_mask:0xf bank_mask:0xf
	v_add_f32_dpp v144, v144, v144 row_ror:8 row_mask:0xf bank_mask:0xf
	v_add_f32_dpp v145, v145, v145 row_ror:8 row_mask:0xf bank_mask:0xf
	v_add_f32_dpp v146, v146, v146 row_ror:8 row_mask:0xf bank_mask:0xf
	v_add_f32_dpp v147, v147, v147 row_ror:8 row_mask:0xf bank_mask:0xf
	v_add_f32_dpp v166, v166, v166 row_ror:8 row_mask:0xf bank_mask:0xf
	v_add_f32_dpp v140, v140, v140 row_ror:4 row_mask:0xf bank_mask:0xf
	v_add_f32_dpp v141, v141, v141 row_ror:4 row_mask:0xf bank_mask:0xf
	v_add_f32_dpp v142, v142, v142 row_ror:4 row_mask:0xf bank_mask:0xf
	v_add_f32_dpp v143, v143, v143 row_ror:4 row_mask:0xf bank_mask:0xf
	v_add_f32_dpp v144, v144, v144 row_ror:4 row_mask:0xf bank_mask:0xf
	v_add_f32_dpp v145, v145, v145 row_ror:4 row_mask:0xf bank_mask:0xf
	v_add_f32_dpp v146, v146, v146 row_ror:4 row_mask:0xf bank_mask:0xf
	v_add_f32_dpp v147, v147, v147 row_ror:4 row_mask:0xf bank_mask:0xf
	v_add_f32_dpp v166, v166, v166 row_ror:4 row_mask:0xf bank_mask:0xf
	v_add_f32_dpp v140, v140, v140 row_ror:2 row_mask:0xf bank_mask:0xf
	v_add_f32_dpp v141, v141, v141 row_ror:2 row_mask:0xf bank_mask:0xf
	v_add_f32_dpp v142, v142, v142 row_ror:2 row_mask:0xf bank_mask:0xf
	v_add_f32_dpp v143, v143, v143 row_ror:2 row_mask:0xf bank_mask:0xf
	v_add_f32_dpp v144, v144, v144 row_ror:2 row_mask:0xf bank_mask:0xf
	v_add_f32_dpp v145, v145, v145 row_ror:2 row_mask:0xf bank_mask:0xf
	v_add_f32_dpp v146, v146, v146 row_ror:2 row_mask:0xf bank_mask:0xf
	v_add_f32_dpp v147, v147, v147 row_ror:2 row_mask:0xf bank_mask:0xf
	v_add_f32_dpp v166, v166, v166 row_ror:2 row_mask:0xf bank_mask:0xf
	v_add_f32_dpp v140, v140, v140 row_ror:1 row_mask:0xf bank_mask:0xf
	v_add_f32_dpp v141, v141, v141 row_ror:1 row_mask:0xf bank_mask:0xf
	v_add_f32_dpp v142, v142, v142 row_ror:1 row_mask:0xf bank_mask:0xf
	v_add_f32_dpp v143, v143, v143 row_ror:1 row_mask:0xf bank_mask:0xf
	v_add_f32_dpp v144, v144, v144 row_ror:1 row_mask:0xf bank_mask:0xf
	v_add_f32_dpp v145, v145, v145 row_ror:1 row_mask:0xf bank_mask:0xf
	v_add_f32_dpp v146, v146, v146 row_ror:1 row_mask:0xf bank_mask:0xf
	v_add_f32_dpp v147, v147, v147 row_ror:1 row_mask:0xf bank_mask:0xf
	v_add_f32_dpp v166, v166, v166 row_ror:1 row_mask:0xf bank_mask:0xf
	v_cvt_pk_f16_f32 v252, v140, v141
	v_cvt_pk_f16_f32 v253, v142, v143
	v_cvt_pk_f16_f32 v254, v144, v145
	v_cvt_pk_f16_f32 v255, v146, v147
	s_waitcnt lgkmcnt(0)
	v_add_f32_e32 v209, s12, v166
	v_add_u32_e32 v220, s18, v102
	v_add_u32_e32 v220, s18, v220
	v_min_u32_e32 v218, s19, v220
	v_lshlrev_b32_e32 v218, 9, v218
	v_lshl_add_u64 v[216:217], v[222:223], 0, v[218:219]
	global_load_dword v228, v[216:217], off nt
	global_load_dword v229, v[216:217], off offset:128 nt
	global_load_dword v230, v[216:217], off offset:256 nt
	global_load_dword v231, v[216:217], off offset:384 nt
	v_add_u32_e32 v220, s18, v220
	v_min_u32_e32 v218, s19, v220
	v_lshlrev_b32_e32 v218, 9, v218
	v_lshl_add_u64 v[216:217], v[222:223], 0, v[218:219]
	global_load_dword v232, v[216:217], off nt
	global_load_dword v233, v[216:217], off offset:128 nt
	global_load_dword v234, v[216:217], off offset:256 nt
	global_load_dword v235, v[216:217], off offset:384 nt
	v_add_u32_e32 v220, s18, v220
	v_min_u32_e32 v218, s19, v220
	v_lshlrev_b32_e32 v218, 9, v218
	v_lshl_add_u64 v[216:217], v[222:223], 0, v[218:219]
	global_load_dword v236, v[216:217], off nt
	global_load_dword v237, v[216:217], off offset:128 nt
	global_load_dword v238, v[216:217], off offset:256 nt
	global_load_dword v239, v[216:217], off offset:384 nt
	v_add_u32_e32 v220, s18, v220
	v_min_u32_e32 v218, s19, v220
	v_lshlrev_b32_e32 v218, 9, v218
	v_lshl_add_u64 v[216:217], v[222:223], 0, v[218:219]
	global_load_dword v240, v[216:217], off nt
	global_load_dword v241, v[216:217], off offset:128 nt
	global_load_dword v242, v[216:217], off offset:256 nt
	global_load_dword v243, v[216:217], off offset:384 nt
	v_add_u32_e32 v220, s18, v220
	v_min_u32_e32 v218, s19, v220
	v_lshlrev_b32_e32 v218, 9, v218
	v_lshl_add_u64 v[216:217], v[222:223], 0, v[218:219]
	global_load_dword v244, v[216:217], off nt
	global_load_dword v245, v[216:217], off offset:128 nt
	global_load_dword v246, v[216:217], off offset:256 nt
	global_load_dword v247, v[216:217], off offset:384 nt
	v_add_u32_e32 v220, s18, v220
	v_min_u32_e32 v218, s19, v220
	v_lshlrev_b32_e32 v218, 9, v218
	v_lshl_add_u64 v[216:217], v[222:223], 0, v[218:219]
	global_load_dword v248, v[216:217], off nt
	global_load_dword v249, v[216:217], off offset:128 nt
	global_load_dword v250, v[216:217], off offset:256 nt
	global_load_dword v251, v[216:217], off offset:384 nt
	s_waitcnt vmcnt(24)

	.amdhsa_kernel _Z5k_decPKiPKDF16_S2_PKfS4_S4_Pf
		.amdhsa_group_segment_fixed_size 47104
		.amdhsa_private_segment_fixed_size 0
		.amdhsa_kernarg_size 312
		.amdhsa_user_sgpr_count 2
		.amdhsa_user_sgpr_dispatch_ptr 0
		.amdhsa_user_sgpr_queue_ptr 0
		.amdhsa_user_sgpr_kernarg_segment_ptr 1
		.amdhsa_user_sgpr_dispatch_id 0
		.amdhsa_user_sgpr_kernarg_preload_length 0
		.amdhsa_user_sgpr_kernarg_preload_offset 0
		.amdhsa_user_sgpr_private_segment_size 0
		.amdhsa_uses_dynamic_stack 0
		.amdhsa_enable_private_segment 0
		.amdhsa_system_sgpr_workgroup_id_x 1
		.amdhsa_system_sgpr_workgroup_id_y 0
		.amdhsa_system_sgpr_workgroup_id_z 0
		.amdhsa_system_sgpr_workgroup_info 0
		.amdhsa_system_vgpr_workitem_id 0
		.amdhsa_next_free_vgpr 256
		.amdhsa_next_free_sgpr 96
		.amdhsa_accum_offset 256
		.amdhsa_reserve_vcc 1
		.amdhsa_float_round_mode_32 0
		.amdhsa_float_round_mode_16_64 0
		.amdhsa_float_denorm_mode_32 3
		.amdhsa_float_denorm_mode_16_64 3
		.amdhsa_dx10_clamp 1
		.amdhsa_ieee_mode 1
		.amdhsa_fp16_overflow 0
		.amdhsa_tg_split 0
		.amdhsa_exception_fp_ieee_invalid_op 0
		.amdhsa_exception_fp_denorm_src 0
		.amdhsa_exception_fp_ieee_div_zero 0
		.amdhsa_exception_fp_ieee_overflow 0
		.amdhsa_exception_fp_ieee_underflow 0
		.amdhsa_exception_fp_ieee_inexact 0
		.amdhsa_exception_int_div_zero 0
	.end_amdhsa_kernel

amdhsa.kernels:
  - .agpr_count:     0
    .args:
      - .actual_access:  read_only
        .address_space:  global
        .offset:         0
        .size:           8
        .value_kind:     global_buffer
      - .actual_access:  read_only
        .address_space:  global
        .offset:         8
        .size:           8
        .value_kind:     global_buffer
      - .actual_access:  write_only
        .address_space:  global
        .offset:         16
        .size:           8
        .value_kind:     global_buffer
      - .actual_access:  read_only
        .address_space:  global
        .offset:         24
        .size:           8
        .value_kind:     global_buffer
      - .actual_access:  write_only
        .address_space:  global
        .offset:         32
        .size:           8
        .value_kind:     global_buffer
      - .actual_access:  write_only
        .address_space:  global
        .offset:         40
        .size:           8
        .value_kind:     global_buffer
      - .actual_access:  read_only
        .address_space:  global
        .offset:         48
        .size:           8
        .value_kind:     global_buffer
      - .actual_access:  read_only
        .address_space:  global
        .offset:         56
        .size:           8
        .value_kind:     global_buffer
      - .actual_access:  write_only
        .address_space:  global
        .offset:         64
        .size:           8
        .value_kind:     global_buffer
    .group_segment_fixed_size: 53904
    .kernarg_segment_align: 8
    .kernarg_segment_size: 72
    .language:       OpenCL C
    .language_version:
      - 2
      - 0
    .max_flat_workgroup_size: 1024
    .name:           _Z6k_partPKiS0_PiS1_PjS1_PKfS4_Pf
    .private_segment_fixed_size: 0
    .sgpr_count:     31
    .sgpr_spill_count: 0
    .symbol:         _Z6k_partPKiS0_PiS1_PjS1_PKfS4_Pf.kd
    .uniform_work_group_size: 1
    .uses_dynamic_stack: false
    .vgpr_count:     64
    .vgpr_spill_count: 0
    .wavefront_size: 64
  - .agpr_count:     0
    .args:
      - .actual_access:  read_only
        .address_space:  global
        .offset:         0
        .size:           8
        .value_kind:     global_buffer
      - .actual_access:  read_only
        .address_space:  global
        .offset:         8
        .size:           8
        .value_kind:     global_buffer
      - .actual_access:  read_only
        .address_space:  global
        .offset:         16
        .size:           8
        .value_kind:     global_buffer
      - .address_space:  global
        .offset:         24
        .size:           8
        .value_kind:     global_buffer
      - .actual_access:  read_only
        .address_space:  global
        .offset:         32
        .size:           8
        .value_kind:     global_buffer
      - .actual_access:  write_only
        .address_space:  global
        .offset:         40
        .size:           8
        .value_kind:     global_buffer
      - .actual_access:  write_only
        .address_space:  global
        .offset:         48
        .size:           8
        .value_kind:     global_buffer
      - .actual_access:  write_only
        .address_space:  global
        .offset:         56
        .size:           8
        .value_kind:     global_buffer
      - .actual_access:  write_only
        .address_space:  global
        .offset:         64
        .size:           8
        .value_kind:     global_buffer
      - .actual_access:  write_only
        .address_space:  global
        .offset:         72
        .size:           8
        .value_kind:     global_buffer
      - .actual_access:  read_only
        .address_space:  global
        .offset:         80
        .size:           8
        .value_kind:     global_buffer
      - .actual_access:  read_only
        .address_space:  global
        .offset:         88
        .size:           8
        .value_kind:     global_buffer
      - .actual_access:  read_only
        .address_space:  global
        .offset:         96
        .size:           8
        .value_kind:     global_buffer
      - .actual_access:  read_only
        .address_space:  global
        .offset:         104
        .size:           8
        .value_kind:     global_buffer
      - .actual_access:  write_only
        .address_space:  global
        .offset:         112
        .size:           8
        .value_kind:     global_buffer
      - .actual_access:  write_only
        .address_space:  global
        .offset:         120
        .size:           8
        .value_kind:     global_buffer
    .group_segment_fixed_size: 38940
    .kernarg_segment_align: 8
    .kernarg_segment_size: 128
    .language:       OpenCL C
    .language_version:
      - 2
      - 0
    .max_flat_workgroup_size: 1024
    .name:           _Z5k_csrPKjPKiS2_PiPKfPfPDF16_S3_S3_S3_S5_S5_S5_S5_S7_S6_
    .private_segment_fixed_size: 0
    .sgpr_count:     72
    .sgpr_spill_count: 0
    .symbol:         _Z5k_csrPKjPKiS2_PiPKfPfPDF16_S3_S3_S3_S5_S5_S5_S5_S7_S6_.kd
    .uniform_work_group_size: 1
    .uses_dynamic_stack: false
    .vgpr_count:     64
    .vgpr_spill_count: 0
    .wavefront_size: 64
  - .agpr_count:     0
    .args:
      - .actual_access:  read_only
        .address_space:  global
        .offset:         0
        .size:           8
        .value_kind:     global_buffer
      - .actual_access:  read_only
        .address_space:  global
        .offset:         8
        .size:           8
        .value_kind:     global_buffer
      - .actual_access:  read_only
        .address_space:  global
        .offset:         16
        .size:           8
        .value_kind:     global_buffer
      - .actual_access:  read_only
        .address_space:  global
        .offset:         24
        .size:           8
        .value_kind:     global_buffer
      - .actual_access:  read_only
        .address_space:  global
        .offset:         32
        .size:           8
        .value_kind:     global_buffer
      - .actual_access:  read_only
        .address_space:  global
        .offset:         40
        .size:           8
        .value_kind:     global_buffer
      - .actual_access:  write_only
        .address_space:  global
        .offset:         48
        .size:           8
        .value_kind:     global_buffer
      - .offset:         56
        .size:           4
        .value_kind:     hidden_block_count_x
      - .offset:         60
        .size:           4
        .value_kind:     hidden_block_count_y
      - .offset:         64
        .size:           4
        .value_kind:     hidden_block_count_z
      - .offset:         68
        .size:           2
        .value_kind:     hidden_group_size_x
      - .offset:         70
        .size:           2
        .value_kind:     hidden_group_size_y
      - .offset:         72
        .size:           2
        .value_kind:     hidden_group_size_z
      - .offset:         74
        .size:           2
        .value_kind:     hidden_remainder_x
      - .offset:         76
        .size:           2
        .value_kind:     hidden_remainder_y
      - .offset:         78
        .size:           2
        .value_kind:     hidden_remainder_z
      - .offset:         96
        .size:           8
        .value_kind:     hidden_global_offset_x
      - .offset:         104
        .size:           8
        .value_kind:     hidden_global_offset_y
      - .offset:         112
        .size:           8
        .value_kind:     hidden_global_offset_z
      - .offset:         120
        .size:           2
        .value_kind:     hidden_grid_dims
    .group_segment_fixed_size: 47104
    .kernarg_segment_align: 8
    .kernarg_segment_size: 312
    .language:       OpenCL C
    .language_version:
      - 2
      - 0
    .max_flat_workgroup_size: 256
    .name:           _Z5k_decPKiPKDF16_S2_PKfS4_S4_Pf
    .private_segment_fixed_size: 0
    .sgpr_count:     28
    .sgpr_spill_count: 0
    .symbol:         _Z5k_decPKiPKDF16_S2_PKfS4_S4_Pf.kd
    .uniform_work_group_size: 1
    .uses_dynamic_stack: false
    .vgpr_count:     256
    .vgpr_spill_count: 0
    .wavefront_size: 64
  - .agpr_count:     0
    .args:
      - .actual_access:  read_only
        .address_space:  global
        .offset:         0
        .size:           8
        .value_kind:     global_buffer
      - .actual_access:  read_only
        .address_space:  global
        .offset:         8
        .size:           8
        .value_kind:     global_buffer
      - .actual_access:  read_only
        .address_space:  global
        .offset:         16
        .size:           8
        .value_kind:     global_buffer
      - .actual_access:  read_only
        .address_space:  global
        .offset:         24
        .size:           8
        .value_kind:     global_buffer
      - .actual_access:  read_only
        .address_space:  global
        .offset:         32
        .size:           8
        .value_kind:     global_buffer
      - .actual_access:  read_only
        .address_space:  global
        .offset:         40
        .size:           8
        .value_kind:     global_buffer
      - .actual_access:  write_only
        .address_space:  global
        .offset:         48
        .size:           8
        .value_kind:     global_buffer
      - .actual_access:  read_only
        .address_space:  global
        .offset:         56
        .size:           8
        .value_kind:     global_buffer
    .group_segment_fixed_size: 0
    .kernarg_segment_align: 8
    .kernarg_segment_size: 64
    .language:       OpenCL C
    .language_version:
      - 2
      - 0
    .max_flat_workgroup_size: 64
    .name:           _Z5k_aggILi1EEvPKiS1_S1_PKDv4_jPKfS6_PS2_PDF16_
    .private_segment_fixed_size: 0
    .sgpr_count:     82
    .sgpr_spill_count: 0
    .symbol:         _Z5k_aggILi1EEvPKiS1_S1_PKDv4_jPKfS6_PS2_PDF16_.kd
    .uniform_work_group_size: 1
    .uses_dynamic_stack: false
    .vgpr_count:     72
    .vgpr_spill_count: 0
    .wavefront_size: 64
  - .agpr_count:     0
    .args:
      - .actual_access:  read_only
        .address_space:  global
        .offset:         0
        .size:           8
        .value_kind:     global_buffer
      - .actual_access:  read_only
        .address_space:  global
        .offset:         8
        .size:           8
        .value_kind:     global_buffer
      - .actual_access:  read_only
        .address_space:  global
        .offset:         16
        .size:           8
        .value_kind:     global_buffer
      - .actual_access:  read_only
        .address_space:  global
        .offset:         24
        .size:           8
        .value_kind:     global_buffer
      - .actual_access:  read_only
        .address_space:  global
        .offset:         32
        .size:           8
        .value_kind:     global_buffer
      - .actual_access:  read_only
        .address_space:  global
        .offset:         40
        .size:           8
        .value_kind:     global_buffer
      - .actual_access:  read_only
        .address_space:  global
        .offset:         48
        .size:           8
        .value_kind:     global_buffer
      - .actual_access:  write_only
        .address_space:  global
        .offset:         56
        .size:           8
        .value_kind:     global_buffer
    .group_segment_fixed_size: 0
    .kernarg_segment_align: 8
    .kernarg_segment_size: 64
    .language:       OpenCL C
    .language_version:
      - 2
      - 0
    .max_flat_workgroup_size: 64
    .name:           _Z5k_aggILi2EEvPKiS1_S1_PKDv4_jPKfS6_PS2_PDF16_
    .private_segment_fixed_size: 0
    .sgpr_count:     66
    .sgpr_spill_count: 0
    .symbol:         _Z5k_aggILi2EEvPKiS1_S1_PKDv4_jPKfS6_PS2_PDF16_.kd
    .uniform_work_group_size: 1
    .uses_dynamic_stack: false
    .vgpr_count:     72
    .vgpr_spill_count: 0
    .wavefront_size: 64
